# P5 LN1 row loop: next row's 16 loads issued right after the current row's staging copies (same staging registers), waits counted past the 24 stores
# baseline (speedup 1.0000x reference)
; __device__ __forceinline__ float bflo(unsigned w) { return __uint_as_float(w << 16); }
; __device__ __forceinline__ float bfhi(unsigned w) { return __uint_as_float(w & 0xffff0000u); }
; template <int MAP>
; __device__ __forceinline__ void ln_finish(float (&v)[32], const float* __restrict__ g, const float* __restrict__ b, float* xout, bf16* xbout, int lane, bf16* xlout = nullptr, unsigned char* x8out = nullptr, unsigned char* xi8out = nullptr, float* sxout = nullptr) {
;     float s = 0.f;
; #pragma unroll
;     for (int i = 0; i < 32; ++i) s += v[i];
;     const float mean = wave_sum(s, lane) * (1.0f / D);
;     float q = 0.f;
; #pragma unroll
;     for (int i = 0; i < 32; ++i) { v[i] -= mean; q += v[i] * v[i]; }
;     const float rstd = 1.0f / sqrtf(wave_sum(q, lane) * (1.0f / D) + LN_EPS);
;     const bool two = (xi8out != nullptr);
;     float qm = 0.f;
;     if (two) {
;         float am = 0.f;
;         if (MAP == 0) {
; #pragma unroll
;             for (int j = 0; j < 8; ++j) { const int c = 4 * (lane + 64 * j); const f32x4 gv = *(const f32x4*)(g + c), bv = *(const f32x4*)(b + c);
;                 v[4 * j] = v[4 * j] * rstd * gv.x + bv.x; v[4 * j + 1] = v[4 * j + 1] * rstd * gv.y + bv.y; v[4 * j + 2] = v[4 * j + 2] * rstd * gv.z + bv.z; v[4 * j + 3] = v[4 * j + 3] * rstd * gv.w + bv.w; }
; __device__ __forceinline__ void ln1_router_unit(const Params& p, int l, int unit, LAS unsigned char* lds, int tid, bool dry = false) {
;     ...
;     for (int r = 0; r < 4; ++r) {
;         const int t = t0 + wid * 4 + r; float v[32]; const bf16* xr = XB + (size_t)t * D; const bf16* mr = MIX + (size_t)t * D;
; #pragma unroll
;         for (int j = 0; j < 8; ++j) { const int c = 4 * (lane + 64 * j); const u32x2 a = __builtin_nontemporal_load((const u32x2*)(xr + c)); const u32x2 mw = __builtin_nontemporal_load((const u32x2*)(mr + c));
;             v[4 * j] = ALPHA * bflo(a.x) + bflo(mw.x); v[4 * j + 1] = ALPHA * bfhi(a.x) + bfhi(mw.x); v[4 * j + 2] = ALPHA * bflo(a.y) + bflo(mw.y); v[4 * j + 3] = ALPHA * bfhi(a.y) + bfhi(mw.y); }
.LBB0_871:
	global_load_dwordx4 v[4:7], v[52:53], off
	global_load_dwordx4 v[8:11], v[50:51], off
	global_load_dwordx4 v[12:15], v[52:53], off offset:1024
	global_load_dwordx4 v[16:19], v[50:51], off offset:1024
	global_load_dwordx4 v[20:23], v[52:53], off offset:2048
	global_load_dwordx4 v[24:27], v[50:51], off offset:2048
	global_load_dwordx4 v[28:31], v[52:53], off offset:3072
	global_load_dwordx4 v[32:35], v[50:51], off offset:3072
	global_load_dwordx4 v[36:39], v[56:57], off
	global_load_dwordx4 v[40:43], v[54:55], off
	global_load_dwordx4 v[44:47], v[60:61], off
	global_load_dwordx4 v[96:99], v[58:59], off
	global_load_dwordx4 v[100:103], v[66:67], off
	global_load_dwordx4 v[104:107], v[62:63], off
	global_load_dwordx4 v[108:111], v[70:71], off
	global_load_dwordx4 v[112:115], v[68:69], off
	v_readfirstlane_b32 s9, v48
	s_ashr_i32 s8, s9, 6
	s_lshl_b32 s6, s8, 2
	v_writelane_b32 v255, s7, 32
	s_add_i32 s6, s7, s6
	s_mov_b32 s7, 0
	s_mov_b32 s88, 0xf800000
	s_waitcnt vmcnt(0)
	v_mov_b32_e32 v0, v4
	v_mov_b32_e32 v1, v7
	v_mov_b32_e32 v2, v8
	v_mov_b32_e32 v3, v11
	v_mov_b32_e32 v4, v5
	v_mov_b32_e32 v5, v6
	v_mov_b32_e32 v6, v9
	v_mov_b32_e32 v7, v10
	v_mov_b32_e32 v8, v12
	v_mov_b32_e32 v9, v15
	v_mov_b32_e32 v10, v16
	v_mov_b32_e32 v11, v19
	v_mov_b32_e32 v12, v13
	v_mov_b32_e32 v13, v14
	v_mov_b32_e32 v14, v17
	v_mov_b32_e32 v15, v18
	v_mov_b32_e32 v16, v20
	v_mov_b32_e32 v17, v23
	v_mov_b32_e32 v18, v24
	v_mov_b32_e32 v19, v27
	v_mov_b32_e32 v20, v21
	v_mov_b32_e32 v21, v22
	v_mov_b32_e32 v22, v25
	v_mov_b32_e32 v23, v26
	v_mov_b32_e32 v24, v28
	v_mov_b32_e32 v25, v31
	v_mov_b32_e32 v26, v32
	v_mov_b32_e32 v27, v35
	v_mov_b32_e32 v28, v29
	v_mov_b32_e32 v29, v30
	v_mov_b32_e32 v30, v33
	v_mov_b32_e32 v31, v34
	v_mov_b32_e32 v32, v36
	v_mov_b32_e32 v33, v39
	v_mov_b32_e32 v34, v40
	v_mov_b32_e32 v35, v43
	v_mov_b32_e32 v36, v37
	v_mov_b32_e32 v37, v38
	v_mov_b32_e32 v38, v41
	v_mov_b32_e32 v39, v42
	v_mov_b32_e32 v40, v44
	v_mov_b32_e32 v41, v47
	v_mov_b32_e32 v42, v96
	v_mov_b32_e32 v43, v99
	v_mov_b32_e32 v44, v45
	v_mov_b32_e32 v45, v46
	v_mov_b32_e32 v46, v97
	v_mov_b32_e32 v47, v98
	v_mov_b32_e32 v96, v100
	v_mov_b32_e32 v97, v103
	v_mov_b32_e32 v98, v104
	v_mov_b32_e32 v99, v107
	v_mov_b32_e32 v100, v101
	v_mov_b32_e32 v101, v102
	v_mov_b32_e32 v102, v105
	v_mov_b32_e32 v103, v106
	v_mov_b32_e32 v104, v108
	v_mov_b32_e32 v105, v111
	v_mov_b32_e32 v106, v112
	v_mov_b32_e32 v107, v115
	v_mov_b32_e32 v108, v109
	v_mov_b32_e32 v109, v110
	v_mov_b32_e32 v110, v113
	v_mov_b32_e32 v111, v114
	s_add_i32 s80, s6, s7
	s_ashr_i32 s81, s80, 31
	s_lshl_b64 s[80:81], s[80:81], 12
	v_lshl_add_u64 v[240:241], v[80:81], 0, s[80:81]
	v_lshl_add_u64 v[242:243], v[82:83], 0, s[80:81]
	global_load_dwordx2 v[198:199], v[240:241], off nt
	global_load_dwordx2 v[200:201], v[242:243], off nt
	global_load_dwordx2 v[202:203], v[240:241], off offset:512 nt
	global_load_dwordx2 v[204:205], v[242:243], off offset:512 nt
	global_load_dwordx2 v[206:207], v[240:241], off offset:1024 nt
	global_load_dwordx2 v[208:209], v[242:243], off offset:1024 nt
	global_load_dwordx2 v[210:211], v[240:241], off offset:1536 nt
	global_load_dwordx2 v[212:213], v[242:243], off offset:1536 nt
	global_load_dwordx2 v[214:215], v[240:241], off offset:2048 nt
	global_load_dwordx2 v[216:217], v[242:243], off offset:2048 nt
	global_load_dwordx2 v[218:219], v[240:241], off offset:2560 nt
	global_load_dwordx2 v[220:221], v[242:243], off offset:2560 nt
	global_load_dwordx2 v[232:233], v[240:241], off offset:3072 nt
	global_load_dwordx2 v[234:235], v[242:243], off offset:3072 nt
	global_load_dwordx2 v[236:237], v[240:241], off offset:3584 nt
	global_load_dwordx2 v[238:239], v[242:243], off offset:3584 nt
	s_waitcnt vmcnt(0)
.LBB0_872:
	s_add_i32 s12, s6, s7
	s_ashr_i32 s13, s12, 31
	s_lshl_b64 s[14:15], s[12:13], 11
	s_lshl_b64 s[12:13], s[12:13], 12
	v_lshl_add_u64 v[114:115], v[80:81], 0, s[12:13]
	v_lshl_add_u64 v[116:117], v[82:83], 0, s[12:13]
	s_waitcnt vmcnt(39)
	v_mov_b64_e32 v[112:113], v[198:199]
	s_waitcnt vmcnt(38)
	v_mov_b64_e32 v[118:119], v[200:201]
	s_add_i32 s7, s7, 1
	s_cmp_eq_u32 s7, 4
	v_lshlrev_b32_e32 v120, 16, v112
	v_lshlrev_b32_e32 v122, 16, v118
	v_and_b32_e32 v126, 0xffff0000, v112
	v_and_b32_e32 v128, 0xffff0000, v118
	v_lshlrev_b32_e32 v127, 16, v113
	v_lshlrev_b32_e32 v129, 16, v119
	v_and_b32_e32 v121, 0xffff0000, v113
	v_and_b32_e32 v123, 0xffff0000, v119
	s_waitcnt vmcnt(37)
	v_mov_b64_e32 v[112:113], v[202:203]
	s_waitcnt vmcnt(36)
	v_mov_b64_e32 v[118:119], v[204:205]
	v_pk_fma_f32 v[120:121], v[120:121], s[96:97], v[122:123] op_sel_hi:[1,0,1]
	v_pk_fma_f32 v[126:127], v[126:127], s[96:97], v[128:129] op_sel_hi:[1,0,1]
	v_add_f32_e32 v91, 0, v120
	v_add_f32_e32 v91, v126, v91
	v_add_f32_e32 v91, v127, v91
	v_add_f32_e32 v91, v121, v91
	v_lshlrev_b32_e32 v130, 16, v112
	v_lshlrev_b32_e32 v132, 16, v118
	v_and_b32_e32 v134, 0xffff0000, v112
	v_and_b32_e32 v136, 0xffff0000, v118
	v_lshlrev_b32_e32 v135, 16, v113
	v_lshlrev_b32_e32 v137, 16, v119
	v_and_b32_e32 v131, 0xffff0000, v113
	v_and_b32_e32 v133, 0xffff0000, v119
	s_waitcnt vmcnt(35)
	v_mov_b64_e32 v[112:113], v[206:207]
	s_waitcnt vmcnt(34)
	v_mov_b64_e32 v[118:119], v[208:209]
	v_pk_fma_f32 v[130:131], v[130:131], s[96:97], v[132:133] op_sel_hi:[1,0,1]
	v_pk_fma_f32 v[128:129], v[134:135], s[96:97], v[136:137] op_sel_hi:[1,0,1]
	v_add_f32_e32 v91, v130, v91
	v_add_f32_e32 v91, v128, v91
	v_add_f32_e32 v91, v129, v91
	v_add_f32_e32 v91, v131, v91
	v_lshlrev_b32_e32 v138, 16, v112
	v_lshlrev_b32_e32 v140, 16, v118
	v_and_b32_e32 v142, 0xffff0000, v112
	v_and_b32_e32 v144, 0xffff0000, v118
	v_lshlrev_b32_e32 v143, 16, v113
	v_lshlrev_b32_e32 v145, 16, v119
	v_and_b32_e32 v139, 0xffff0000, v113
	v_and_b32_e32 v141, 0xffff0000, v119
	s_waitcnt vmcnt(33)
; __device__ __forceinline__ float bflo(unsigned w) { return __uint_as_float(w << 16); }
; __device__ __forceinline__ float bfhi(unsigned w) { return __uint_as_float(w & 0xffff0000u); }
; template <int MAP>
; __device__ __forceinline__ void ln_finish(float (&v)[32], const float* __restrict__ g, const float* __restrict__ b, float* xout, bf16* xbout, int lane, bf16* xlout = nullptr, unsigned char* x8out = nullptr, unsigned char* xi8out = nullptr, float* sxout = nullptr) {
;     float s = 0.f;
; #pragma unroll
;     for (int i = 0; i < 32; ++i) s += v[i];
;     const float mean = wave_sum(s, lane) * (1.0f / D);
; __device__ __forceinline__ void ln1_router_unit(const Params& p, int l, int unit, LAS unsigned char* lds, int tid, bool dry = false) {
;     ...
;     for (int r = 0; r < 4; ++r) {
;         const int t = t0 + wid * 4 + r; float v[32]; const bf16* xr = XB + (size_t)t * D; const bf16* mr = MIX + (size_t)t * D;
; #pragma unroll
;         for (int j = 0; j < 8; ++j) { const int c = 4 * (lane + 64 * j); const u32x2 a = __builtin_nontemporal_load((const u32x2*)(xr + c)); const u32x2 mw = __builtin_nontemporal_load((const u32x2*)(mr + c));
;             v[4 * j] = ALPHA * bflo(a.x) + bflo(mw.x); v[4 * j + 1] = ALPHA * bfhi(a.x) + bfhi(mw.x); v[4 * j + 2] = ALPHA * bflo(a.y) + bflo(mw.y); v[4 * j + 3] = ALPHA * bfhi(a.y) + bfhi(mw.y); }
	v_mov_b64_e32 v[112:113], v[210:211]
	s_waitcnt vmcnt(32)
	v_mov_b64_e32 v[118:119], v[212:213]
	v_pk_fma_f32 v[134:135], v[138:139], s[96:97], v[140:141] op_sel_hi:[1,0,1]
	v_pk_fma_f32 v[132:133], v[142:143], s[96:97], v[144:145] op_sel_hi:[1,0,1]
	v_add_f32_e32 v91, v134, v91
	v_add_f32_e32 v91, v132, v91
	v_add_f32_e32 v91, v133, v91
	v_add_f32_e32 v91, v135, v91
	v_lshlrev_b32_e32 v146, 16, v112
	v_lshlrev_b32_e32 v148, 16, v118
	v_and_b32_e32 v168, 0xffff0000, v112
	v_and_b32_e32 v170, 0xffff0000, v118
	v_lshlrev_b32_e32 v169, 16, v113
	v_lshlrev_b32_e32 v171, 16, v119
	v_and_b32_e32 v147, 0xffff0000, v113
	v_and_b32_e32 v149, 0xffff0000, v119
	s_waitcnt vmcnt(31)
	v_mov_b64_e32 v[112:113], v[214:215]
	s_waitcnt vmcnt(30)
	v_mov_b64_e32 v[118:119], v[216:217]
	v_pk_fma_f32 v[138:139], v[146:147], s[96:97], v[148:149] op_sel_hi:[1,0,1]
	v_pk_fma_f32 v[136:137], v[168:169], s[96:97], v[170:171] op_sel_hi:[1,0,1]
	v_add_f32_e32 v91, v138, v91
	v_add_f32_e32 v91, v136, v91
	v_add_f32_e32 v91, v137, v91
	v_add_f32_e32 v91, v139, v91
	v_lshlrev_b32_e32 v172, 16, v112
	v_lshlrev_b32_e32 v174, 16, v118
	v_and_b32_e32 v176, 0xffff0000, v112
	v_and_b32_e32 v178, 0xffff0000, v118
	v_lshlrev_b32_e32 v177, 16, v113
	v_lshlrev_b32_e32 v179, 16, v119
	v_and_b32_e32 v173, 0xffff0000, v113
	v_and_b32_e32 v175, 0xffff0000, v119
	s_waitcnt vmcnt(29)
	v_mov_b64_e32 v[112:113], v[218:219]
	s_waitcnt vmcnt(28)
	v_mov_b64_e32 v[118:119], v[220:221]
	v_pk_fma_f32 v[170:171], v[172:173], s[96:97], v[174:175] op_sel_hi:[1,0,1]
	v_pk_fma_f32 v[168:169], v[176:177], s[96:97], v[178:179] op_sel_hi:[1,0,1]
	v_add_f32_e32 v91, v170, v91
	v_add_f32_e32 v91, v168, v91
	v_add_f32_e32 v91, v169, v91
	v_add_f32_e32 v91, v171, v91
	v_lshlrev_b32_e32 v180, 16, v112
	v_lshlrev_b32_e32 v182, 16, v118
	v_and_b32_e32 v184, 0xffff0000, v112
	v_and_b32_e32 v186, 0xffff0000, v118
	v_lshlrev_b32_e32 v185, 16, v113
	v_lshlrev_b32_e32 v187, 16, v119
	v_and_b32_e32 v181, 0xffff0000, v113
	v_and_b32_e32 v183, 0xffff0000, v119
	s_waitcnt vmcnt(27)
	v_mov_b64_e32 v[112:113], v[232:233]
	s_waitcnt vmcnt(26)
	v_mov_b64_e32 v[118:119], v[234:235]
	v_pk_fma_f32 v[174:175], v[180:181], s[96:97], v[182:183] op_sel_hi:[1,0,1]
	v_pk_fma_f32 v[172:173], v[184:185], s[96:97], v[186:187] op_sel_hi:[1,0,1]
	v_add_f32_e32 v91, v174, v91
	v_add_f32_e32 v91, v172, v91
	v_add_f32_e32 v91, v173, v91
	v_add_f32_e32 v91, v175, v91
	v_lshlrev_b32_e32 v188, 16, v112
	v_and_b32_e32 v192, 0xffff0000, v112
	v_lshlrev_b32_e32 v193, 16, v113
	v_and_b32_e32 v189, 0xffff0000, v113
	s_waitcnt vmcnt(25)
	v_mov_b64_e32 v[112:113], v[236:237]
	s_nop 0
	s_waitcnt vmcnt(24)
	v_mov_b64_e32 v[116:117], v[238:239]
	s_cbranch_scc1 .Lmy_p5_nopf
	s_add_i32 s80, s6, s7
	s_ashr_i32 s81, s80, 31
	s_lshl_b64 s[80:81], s[80:81], 12
	v_lshl_add_u64 v[240:241], v[80:81], 0, s[80:81]
	v_lshl_add_u64 v[242:243], v[82:83], 0, s[80:81]
	global_load_dwordx2 v[198:199], v[240:241], off nt
	global_load_dwordx2 v[200:201], v[242:243], off nt
	global_load_dwordx2 v[202:203], v[240:241], off offset:512 nt
	global_load_dwordx2 v[204:205], v[242:243], off offset:512 nt
	global_load_dwordx2 v[206:207], v[240:241], off offset:1024 nt
	global_load_dwordx2 v[208:209], v[242:243], off offset:1024 nt
	global_load_dwordx2 v[210:211], v[240:241], off offset:1536 nt
	global_load_dwordx2 v[212:213], v[242:243], off offset:1536 nt
	global_load_dwordx2 v[214:215], v[240:241], off offset:2048 nt
	global_load_dwordx2 v[216:217], v[242:243], off offset:2048 nt
	global_load_dwordx2 v[218:219], v[240:241], off offset:2560 nt
	global_load_dwordx2 v[220:221], v[242:243], off offset:2560 nt
	global_load_dwordx2 v[232:233], v[240:241], off offset:3072 nt
	global_load_dwordx2 v[234:235], v[242:243], off offset:3072 nt
	global_load_dwordx2 v[236:237], v[240:241], off offset:3584 nt
	global_load_dwordx2 v[238:239], v[242:243], off offset:3584 nt
	s_cmp_lg_u32 s7, s7
.Lmy_p5_nopf:
	v_lshlrev_b32_e32 v190, 16, v118
	v_and_b32_e32 v191, 0xffff0000, v119
	v_and_b32_e32 v194, 0xffff0000, v118
	v_lshlrev_b32_e32 v195, 16, v119
	v_pk_fma_f32 v[178:179], v[188:189], s[96:97], v[190:191] op_sel_hi:[1,0,1]
	v_pk_fma_f32 v[176:177], v[192:193], s[96:97], v[194:195] op_sel_hi:[1,0,1]
	v_add_f32_e32 v91, v178, v91
	v_add_f32_e32 v91, v176, v91
	v_add_f32_e32 v91, v177, v91
	v_add_f32_e32 v91, v179, v91
	v_and_b32_e32 v118, 0xffff0000, v112
	v_lshlrev_b32_e32 v119, 16, v112
	v_and_b32_e32 v196, 0xffff0000, v116
	v_lshlrev_b32_e32 v197, 16, v116
	v_pk_fma_f32 v[118:119], v[118:119], s[96:97], v[196:197] op_sel_hi:[1,0,1]
	v_and_b32_e32 v112, 0xffff0000, v113
	v_lshlrev_b32_e32 v113, 16, v113
	v_and_b32_e32 v116, 0xffff0000, v117
	v_lshlrev_b32_e32 v117, 16, v117
	v_add_f32_e32 v91, v119, v91
	v_pk_fma_f32 v[122:123], v[112:113], s[96:97], v[116:117] op_sel_hi:[1,0,1]
	v_add_f32_e32 v91, v118, v91
	v_add_f32_e32 v91, v123, v91
	v_add_f32_e32 v91, v122, v91
	ds_bpermute_b32 v93, v125, v91
	v_lshl_add_u64 v[116:117], v[84:85], 0, s[12:13]
	v_lshl_add_u64 v[112:113], v[86:87], 0, s[14:15]
	s_waitcnt lgkmcnt(0)
	v_add_f32_e32 v91, v91, v93
	ds_bpermute_b32 v93, v150, v91
	s_waitcnt lgkmcnt(0)
	v_add_f32_e32 v91, v91, v93
	ds_bpermute_b32 v93, v151, v91
	s_waitcnt lgkmcnt(0)
	v_add_f32_e32 v91, v91, v93
	ds_bpermute_b32 v93, v152, v91
	s_waitcnt lgkmcnt(0)
	v_add_f32_e32 v91, v91, v93
	ds_bpermute_b32 v93, v153, v91
	s_waitcnt lgkmcnt(0)
	v_add_f32_e32 v91, v91, v93
	ds_bpermute_b32 v93, v154, v91
	s_waitcnt lgkmcnt(0)
; __device__ __forceinline__ unsigned pk2(float lo, float hi) { return f2bf(lo) | (f2bf(hi) << 16); }
; template <int MAP>
; __device__ __forceinline__ void ln_finish(float (&v)[32], const float* __restrict__ g, const float* __restrict__ b, float* xout, bf16* xbout, int lane, bf16* xlout = nullptr, unsigned char* x8out = nullptr, unsigned char* xi8out = nullptr, float* sxout = nullptr) {
;     ...
;     const float mean = wave_sum(s, lane) * (1.0f / D);
;     float q = 0.f;
; #pragma unroll
;     for (int i = 0; i < 32; ++i) { v[i] -= mean; q += v[i] * v[i]; }
;     const float rstd = 1.0f / sqrtf(wave_sum(q, lane) * (1.0f / D) + LN_EPS);
;     ...
;             else { const f32x4 gv = *(const f32x4*)(g + c), bv = *(const f32x4*)(b + c);
;                 o.x = v[4 * j] * rstd * gv.x + bv.x; o.y = v[4 * j + 1] * rstd * gv.y + bv.y; o.z = v[4 * j + 2] * rstd * gv.z + bv.z; o.w = v[4 * j + 3] * rstd * gv.w + bv.w; }
;             if (xout) *(f32x4*)(xout + c) = o;
;             if (xbout) { u32x2 w; w.x = pk2(o.x, o.y); w.y = pk2(o.z, o.w); *(u32x2*)(xbout + c) = w; }
	v_add_f32_e32 v91, v91, v93
	v_mul_f32_e32 v124, 0x3a000000, v91
	v_pk_add_f32 v[180:181], v[120:121], v[124:125] op_sel_hi:[1,0] neg_lo:[0,1] neg_hi:[0,1]
	v_pk_add_f32 v[182:183], v[126:127], v[124:125] op_sel_hi:[1,0] neg_lo:[0,1] neg_hi:[0,1]
	v_pk_mul_f32 v[120:121], v[180:181], v[180:181]
	v_pk_mul_f32 v[184:185], v[182:183], v[182:183]
	v_pk_add_f32 v[146:147], v[130:131], v[124:125] op_sel_hi:[1,0] neg_lo:[0,1] neg_hi:[0,1]
	v_add_f32_e32 v93, v120, v184
	v_add_f32_e32 v93, v185, v93
	v_pk_mul_f32 v[186:187], v[146:147], v[146:147]
	v_pk_add_f32 v[148:149], v[128:129], v[124:125] op_sel_hi:[1,0] neg_lo:[0,1] neg_hi:[0,1]
	v_add_f32_e32 v93, v121, v93
	v_pk_mul_f32 v[188:189], v[148:149], v[148:149]
	v_add_f32_e32 v93, v186, v93
	v_add_f32_e32 v93, v188, v93
	v_pk_add_f32 v[142:143], v[134:135], v[124:125] op_sel_hi:[1,0] neg_lo:[0,1] neg_hi:[0,1]
	v_add_f32_e32 v93, v189, v93
	v_pk_mul_f32 v[190:191], v[142:143], v[142:143]
	v_pk_add_f32 v[144:145], v[132:133], v[124:125] op_sel_hi:[1,0] neg_lo:[0,1] neg_hi:[0,1]
	v_add_f32_e32 v93, v187, v93
	v_pk_mul_f32 v[192:193], v[144:145], v[144:145]
	v_add_f32_e32 v93, v190, v93
	v_add_f32_e32 v93, v192, v93
	v_pk_add_f32 v[138:139], v[138:139], v[124:125] op_sel_hi:[1,0] neg_lo:[0,1] neg_hi:[0,1]
	v_add_f32_e32 v93, v193, v93
	v_pk_mul_f32 v[194:195], v[138:139], v[138:139]
	v_pk_add_f32 v[140:141], v[136:137], v[124:125] op_sel_hi:[1,0] neg_lo:[0,1] neg_hi:[0,1]
	v_add_f32_e32 v93, v191, v93
	v_pk_mul_f32 v[196:197], v[140:141], v[140:141]
	v_add_f32_e32 v93, v194, v93
	v_add_f32_e32 v93, v196, v93
	v_pk_add_f32 v[134:135], v[170:171], v[124:125] op_sel_hi:[1,0] neg_lo:[0,1] neg_hi:[0,1]
	v_add_f32_e32 v93, v197, v93
	v_pk_mul_f32 v[170:171], v[134:135], v[134:135]
	v_pk_add_f32 v[136:137], v[168:169], v[124:125] op_sel_hi:[1,0] neg_lo:[0,1] neg_hi:[0,1]
	v_add_f32_e32 v93, v195, v93
	v_pk_mul_f32 v[168:169], v[136:137], v[136:137]
	v_add_f32_e32 v93, v170, v93
	v_add_f32_e32 v93, v168, v93
	v_pk_add_f32 v[130:131], v[174:175], v[124:125] op_sel_hi:[1,0] neg_lo:[0,1] neg_hi:[0,1]
	v_add_f32_e32 v93, v169, v93
	v_pk_mul_f32 v[174:175], v[130:131], v[130:131]
	v_pk_add_f32 v[132:133], v[172:173], v[124:125] op_sel_hi:[1,0] neg_lo:[0,1] neg_hi:[0,1]
	v_add_f32_e32 v93, v171, v93
	v_pk_mul_f32 v[172:173], v[132:133], v[132:133]
	v_add_f32_e32 v93, v174, v93
	v_add_f32_e32 v93, v172, v93
	v_pk_add_f32 v[126:127], v[178:179], v[124:125] op_sel_hi:[1,0] neg_lo:[0,1] neg_hi:[0,1]
	v_add_f32_e32 v93, v173, v93
	v_pk_mul_f32 v[178:179], v[126:127], v[126:127]
	v_pk_add_f32 v[128:129], v[176:177], v[124:125] op_sel_hi:[1,0] neg_lo:[0,1] neg_hi:[0,1]
	v_add_f32_e32 v93, v175, v93
	v_pk_mul_f32 v[176:177], v[128:129], v[128:129]
	v_add_f32_e32 v93, v178, v93
	v_add_f32_e32 v93, v176, v93
	v_add_f32_e32 v93, v177, v93
	v_add_f32_e32 v93, v179, v93
	v_fmamk_f32 v120, v91, 0xba000000, v119
	v_fmac_f32_e32 v93, v120, v120
	v_fmac_f32_e32 v118, 0xba000000, v91
	v_pk_add_f32 v[122:123], v[122:123], v[124:125] op_sel_hi:[1,0] neg_lo:[0,1] neg_hi:[0,1]
	v_fmac_f32_e32 v93, v118, v118
	v_pk_mul_f32 v[168:169], v[122:123], v[122:123]
	s_nop 0
	v_add_f32_e32 v91, v169, v93
	v_add_f32_e32 v91, v168, v91
	ds_bpermute_b32 v93, v125, v91
	s_waitcnt lgkmcnt(0)
	v_add_f32_e32 v91, v91, v93
	ds_bpermute_b32 v93, v150, v91
	s_waitcnt lgkmcnt(0)
	v_add_f32_e32 v91, v91, v93
	ds_bpermute_b32 v93, v151, v91
	s_waitcnt lgkmcnt(0)
	v_add_f32_e32 v91, v91, v93
	ds_bpermute_b32 v93, v152, v91
	s_waitcnt lgkmcnt(0)
	v_add_f32_e32 v91, v91, v93
	ds_bpermute_b32 v93, v153, v91
	s_waitcnt lgkmcnt(0)
	v_add_f32_e32 v91, v91, v93
	ds_bpermute_b32 v93, v154, v91
	s_waitcnt lgkmcnt(0)
	v_add_f32_e32 v91, v91, v93
	v_fmamk_f32 v91, v91, 0x3a000000, v223
	v_cmp_gt_f32_e32 vcc, s88, v91
	v_mul_f32_e32 v93, 0x4f800000, v91
	s_nop 0
	v_cndmask_b32_e32 v91, v91, v93, vcc
	v_sqrt_f32_e32 v93, v91
	s_nop 0
	v_add_u32_e32 v95, -1, v93
	v_fma_f32 v119, -v95, v93, v91
	v_cmp_ge_f32_e64 s[86:87], 0, v119
	v_add_u32_e32 v119, 1, v93
	s_nop 0
	v_cndmask_b32_e64 v95, v93, v95, s[86:87]
	v_fma_f32 v93, -v119, v93, v91
	v_cmp_lt_f32_e64 s[86:87], 0, v93
	s_nop 1
	v_cndmask_b32_e64 v93, v95, v119, s[86:87]
	v_mul_f32_e32 v95, 0x37800000, v93
	v_cndmask_b32_e32 v93, v93, v95, vcc
	v_cmp_class_f32_e32 vcc, v91, v224
	s_nop 1
	v_cndmask_b32_e32 v91, v93, v91, vcc
	v_div_scale_f32 v93, s[12:13], v91, v91, 1.0
	v_rcp_f32_e32 v95, v93
	s_nop 0
	v_fma_f32 v119, -v93, v95, 1.0
	v_fmac_f32_e32 v95, v119, v95
	v_div_scale_f32 v119, vcc, 1.0, v91, 1.0
	v_mul_f32_e32 v121, v119, v95
	v_fma_f32 v124, -v93, v121, v119
	v_fmac_f32_e32 v121, v124, v95
	v_fma_f32 v93, -v93, v121, v119
	v_div_fmas_f32 v93, v93, v95, v121
	v_div_fixup_f32 v124, v93, v91, 1.0
	v_pk_mul_f32 v[168:169], v[182:183], v[124:125] op_sel_hi:[1,0]
	v_pk_mul_f32 v[170:171], v[180:181], v[124:125] op_sel_hi:[1,0]
	v_pk_fma_f32 v[168:169], v[6:7], v[168:169], v[4:5]
	v_pk_fma_f32 v[170:171], v[2:3], v[170:171], v[0:1]
	v_and_b32_sdwa v93, v168, v222 dst_sel:DWORD dst_unused:UNUSED_PAD src0_sel:WORD_1 src1_sel:DWORD
	v_add3_u32 v93, v168, v93, s30
	v_and_b32_e32 v172, 0xffff0000, v93
	v_and_b32_sdwa v93, v171, v222 dst_sel:DWORD dst_unused:UNUSED_PAD src0_sel:WORD_1 src1_sel:DWORD
	v_and_b32_sdwa v91, v169, v222 dst_sel:DWORD dst_unused:UNUSED_PAD src0_sel:WORD_1 src1_sel:DWORD
	v_and_b32_sdwa v95, v170, v222 dst_sel:DWORD dst_unused:UNUSED_PAD src0_sel:WORD_1 src1_sel:DWORD
	v_add3_u32 v93, v171, v93, s30
	v_add3_u32 v91, v169, v91, s30
	v_add3_u32 v95, v170, v95, s30
	v_and_b32_e32 v173, 0xffff0000, v93
	v_or_b32_sdwa v175, v173, v91 dst_sel:DWORD dst_unused:UNUSED_PAD src0_sel:DWORD src1_sel:WORD_1
; __device__ __forceinline__ float bf2f(unsigned b) { return __uint_as_float(b << 16); }
; __device__ __forceinline__ unsigned f2bf(float f) { unsigned u = __float_as_uint(f); return (u + 0x7fffu + ((u >> 16) & 1u)) >> 16; }
; __device__ __forceinline__ unsigned pk2(float lo, float hi) { return f2bf(lo) | (f2bf(hi) << 16); }
; __device__ __forceinline__ unsigned pk4_fp8(float a, float b, float c, float d) { unsigned w = 0u; w = __builtin_amdgcn_cvt_pk_fp8_f32(clamp8(a), clamp8(b), w, false); w = __builtin_amdgcn_cvt_pk_fp8_f32(clamp8(c), clamp8(d), w, true); return w; }
; template <int MAP>
; __device__ __forceinline__ void ln_finish(float (&v)[32], const float* __restrict__ g, const float* __restrict__ b, float* xout, bf16* xbout, int lane, bf16* xlout = nullptr, unsigned char* x8out = nullptr, unsigned char* xi8out = nullptr, float* sxout = nullptr) {
;     ...
;             else { const f32x4 gv = *(const f32x4*)(g + c), bv = *(const f32x4*)(b + c);
;                 o.x = v[4 * j] * rstd * gv.x + bv.x; o.y = v[4 * j + 1] * rstd * gv.y + bv.y; o.z = v[4 * j + 2] * rstd * gv.z + bv.z; o.w = v[4 * j + 3] * rstd * gv.w + bv.w; }
;             if (xout) *(f32x4*)(xout + c) = o;
;             if (xbout) { u32x2 w; w.x = pk2(o.x, o.y); w.y = pk2(o.z, o.w); *(u32x2*)(xbout + c) = w; }
;             if (xlout) { u32x2 w; w.x = pk2(o.x - bf2f(f2bf(o.x)), o.y - bf2f(f2bf(o.y))); w.y = pk2(o.z - bf2f(f2bf(o.z)), o.w - bf2f(f2bf(o.w))); *(u32x2*)(xlout + c) = w; }
;             if (x8out) *(unsigned*)(x8out + c) = pk4_fp8(o.x, o.y, o.z, o.w);
	v_or_b32_sdwa v174, v95, v172 dst_sel:DWORD dst_unused:UNUSED_PAD src0_sel:WORD_1 src1_sel:DWORD
	global_store_dwordx2 v[114:115], v[174:175], off
	v_and_b32_e32 v175, 0xffff0000, v91
	v_and_b32_e32 v174, 0xffff0000, v95
	v_mov_b32_e32 v176, v170
	v_mov_b32_e32 v177, v169
	v_pk_add_f32 v[174:175], v[176:177], v[174:175] neg_lo:[0,1] neg_hi:[0,1]
	v_mov_b32_e32 v176, v168
	v_mov_b32_e32 v177, v171
	v_pk_add_f32 v[172:173], v[176:177], v[172:173] neg_lo:[0,1] neg_hi:[0,1]
	v_and_b32_sdwa v91, v175, v222 dst_sel:DWORD dst_unused:UNUSED_PAD src0_sel:WORD_1 src1_sel:DWORD
	v_and_b32_sdwa v95, v173, v222 dst_sel:DWORD dst_unused:UNUSED_PAD src0_sel:WORD_1 src1_sel:DWORD
	v_and_b32_sdwa v119, v172, v222 dst_sel:DWORD dst_unused:UNUSED_PAD src0_sel:WORD_1 src1_sel:DWORD
	v_and_b32_sdwa v93, v174, v222 dst_sel:DWORD dst_unused:UNUSED_PAD src0_sel:WORD_1 src1_sel:DWORD
	v_add3_u32 v95, v173, v95, s30
	v_add3_u32 v119, v172, v119, s30
	v_add3_u32 v93, v174, v93, s30
	v_add3_u32 v91, v175, v91, s30
	v_and_b32_e32 v95, 0xffff0000, v95
	v_and_b32_e32 v119, 0xffff0000, v119
	v_or_b32_sdwa v173, v95, v91 dst_sel:DWORD dst_unused:UNUSED_PAD src0_sel:DWORD src1_sel:WORD_1
	v_or_b32_sdwa v172, v119, v93 dst_sel:DWORD dst_unused:UNUSED_PAD src0_sel:DWORD src1_sel:WORD_1
	v_med3_f32 v95, v168, s33, v229
	v_med3_f32 v119, v170, s33, v229
	v_mov_b32_e32 v121, 0
	v_cvt_pk_fp8_f32 v121, v119, v95
	v_pk_mul_f32 v[148:149], v[148:149], v[124:125] op_sel_hi:[1,0]
	v_med3_f32 v91, v171, s33, v229
	v_med3_f32 v93, v169, s33, v229
	v_pk_fma_f32 v[148:149], v[14:15], v[148:149], v[12:13]
	v_cvt_pk_fp8_f32 v121, v93, v91 op_sel:[0,0,1]
	v_pk_mul_f32 v[146:147], v[146:147], v[124:125] op_sel_hi:[1,0]
	v_and_b32_sdwa v93, v148, v222 dst_sel:DWORD dst_unused:UNUSED_PAD src0_sel:WORD_1 src1_sel:DWORD
	v_pk_fma_f32 v[146:147], v[10:11], v[146:147], v[8:9]
	v_add3_u32 v93, v148, v93, s30
	v_and_b32_e32 v168, 0xffff0000, v93
	v_and_b32_sdwa v93, v147, v222 dst_sel:DWORD dst_unused:UNUSED_PAD src0_sel:WORD_1 src1_sel:DWORD
	v_and_b32_sdwa v91, v149, v222 dst_sel:DWORD dst_unused:UNUSED_PAD src0_sel:WORD_1 src1_sel:DWORD
	v_and_b32_sdwa v95, v146, v222 dst_sel:DWORD dst_unused:UNUSED_PAD src0_sel:WORD_1 src1_sel:DWORD
	v_add3_u32 v93, v147, v93, s30
	v_add3_u32 v91, v149, v91, s30
	v_add3_u32 v95, v146, v95, s30
	v_and_b32_e32 v169, 0xffff0000, v93
	v_or_b32_sdwa v171, v169, v91 dst_sel:DWORD dst_unused:UNUSED_PAD src0_sel:DWORD src1_sel:WORD_1
	v_or_b32_sdwa v170, v95, v168 dst_sel:DWORD dst_unused:UNUSED_PAD src0_sel:WORD_1 src1_sel:DWORD
	global_store_dwordx2 v[116:117], v[172:173], off
	global_store_dword v[112:113], v121, off
	global_store_dwordx2 v[114:115], v[170:171], off offset:512
	v_and_b32_e32 v171, 0xffff0000, v91
	v_and_b32_e32 v170, 0xffff0000, v95
	v_mov_b32_e32 v172, v146
	v_mov_b32_e32 v173, v149
	v_pk_add_f32 v[170:171], v[172:173], v[170:171] neg_lo:[0,1] neg_hi:[0,1]
	v_mov_b32_e32 v172, v148
	v_mov_b32_e32 v173, v147
	v_pk_add_f32 v[168:169], v[172:173], v[168:169] neg_lo:[0,1] neg_hi:[0,1]
	v_and_b32_sdwa v91, v171, v222 dst_sel:DWORD dst_unused:UNUSED_PAD src0_sel:WORD_1 src1_sel:DWORD
	v_and_b32_sdwa v95, v169, v222 dst_sel:DWORD dst_unused:UNUSED_PAD src0_sel:WORD_1 src1_sel:DWORD
	v_and_b32_sdwa v119, v168, v222 dst_sel:DWORD dst_unused:UNUSED_PAD src0_sel:WORD_1 src1_sel:DWORD
	v_and_b32_sdwa v93, v170, v222 dst_sel:DWORD dst_unused:UNUSED_PAD src0_sel:WORD_1 src1_sel:DWORD
	v_add3_u32 v95, v169, v95, s30
	v_add3_u32 v119, v168, v119, s30
	v_add3_u32 v93, v170, v93, s30
	v_add3_u32 v91, v171, v91, s30
	v_and_b32_e32 v95, 0xffff0000, v95
	v_and_b32_e32 v119, 0xffff0000, v119
	v_or_b32_sdwa v169, v95, v91 dst_sel:DWORD dst_unused:UNUSED_PAD src0_sel:DWORD src1_sel:WORD_1
	v_or_b32_sdwa v168, v119, v93 dst_sel:DWORD dst_unused:UNUSED_PAD src0_sel:DWORD src1_sel:WORD_1
	v_med3_f32 v95, v148, s33, v229
	v_med3_f32 v119, v146, s33, v229
	v_mov_b32_e32 v121, 0
	v_cvt_pk_fp8_f32 v121, v119, v95
	v_pk_mul_f32 v[144:145], v[144:145], v[124:125] op_sel_hi:[1,0]
	v_med3_f32 v91, v147, s33, v229
	v_med3_f32 v93, v149, s33, v229
	v_pk_fma_f32 v[144:145], v[22:23], v[144:145], v[20:21]
	v_cvt_pk_fp8_f32 v121, v93, v91 op_sel:[0,0,1]
	v_pk_mul_f32 v[142:143], v[142:143], v[124:125] op_sel_hi:[1,0]
	v_and_b32_sdwa v93, v144, v222 dst_sel:DWORD dst_unused:UNUSED_PAD src0_sel:WORD_1 src1_sel:DWORD
	v_pk_fma_f32 v[142:143], v[18:19], v[142:143], v[16:17]
	v_add3_u32 v93, v144, v93, s30
	v_and_b32_e32 v146, 0xffff0000, v93
	v_and_b32_sdwa v93, v143, v222 dst_sel:DWORD dst_unused:UNUSED_PAD src0_sel:WORD_1 src1_sel:DWORD
	v_and_b32_sdwa v91, v145, v222 dst_sel:DWORD dst_unused:UNUSED_PAD src0_sel:WORD_1 src1_sel:DWORD
	v_and_b32_sdwa v95, v142, v222 dst_sel:DWORD dst_unused:UNUSED_PAD src0_sel:WORD_1 src1_sel:DWORD
	v_add3_u32 v93, v143, v93, s30
	v_add3_u32 v91, v145, v91, s30
	v_add3_u32 v95, v142, v95, s30
	v_and_b32_e32 v147, 0xffff0000, v93
	v_or_b32_sdwa v149, v147, v91 dst_sel:DWORD dst_unused:UNUSED_PAD src0_sel:DWORD src1_sel:WORD_1
	v_or_b32_sdwa v148, v95, v146 dst_sel:DWORD dst_unused:UNUSED_PAD src0_sel:WORD_1 src1_sel:DWORD
	global_store_dwordx2 v[116:117], v[168:169], off offset:512
	global_store_dword v[112:113], v121, off offset:256
	global_store_dwordx2 v[114:115], v[148:149], off offset:1024
	v_and_b32_e32 v149, 0xffff0000, v91
	v_and_b32_e32 v148, 0xffff0000, v95
	v_mov_b32_e32 v168, v142
	v_mov_b32_e32 v169, v145
	v_pk_add_f32 v[148:149], v[168:169], v[148:149] neg_lo:[0,1] neg_hi:[0,1]
	v_mov_b32_e32 v168, v144
	v_mov_b32_e32 v169, v143
	v_pk_add_f32 v[146:147], v[168:169], v[146:147] neg_lo:[0,1] neg_hi:[0,1]
; __device__ __forceinline__ float bf2f(unsigned b) { return __uint_as_float(b << 16); }
; __device__ __forceinline__ unsigned f2bf(float f) { unsigned u = __float_as_uint(f); return (u + 0x7fffu + ((u >> 16) & 1u)) >> 16; }
; __device__ __forceinline__ unsigned pk2(float lo, float hi) { return f2bf(lo) | (f2bf(hi) << 16); }
; __device__ __forceinline__ unsigned pk4_fp8(float a, float b, float c, float d) { unsigned w = 0u; w = __builtin_amdgcn_cvt_pk_fp8_f32(clamp8(a), clamp8(b), w, false); w = __builtin_amdgcn_cvt_pk_fp8_f32(clamp8(c), clamp8(d), w, true); return w; }
; template <int MAP>
; __device__ __forceinline__ void ln_finish(float (&v)[32], const float* __restrict__ g, const float* __restrict__ b, float* xout, bf16* xbout, int lane, bf16* xlout = nullptr, unsigned char* x8out = nullptr, unsigned char* xi8out = nullptr, float* sxout = nullptr) {
;     ...
;             else { const f32x4 gv = *(const f32x4*)(g + c), bv = *(const f32x4*)(b + c);
;                 o.x = v[4 * j] * rstd * gv.x + bv.x; o.y = v[4 * j + 1] * rstd * gv.y + bv.y; o.z = v[4 * j + 2] * rstd * gv.z + bv.z; o.w = v[4 * j + 3] * rstd * gv.w + bv.w; }
;             if (xout) *(f32x4*)(xout + c) = o;
;             if (xbout) { u32x2 w; w.x = pk2(o.x, o.y); w.y = pk2(o.z, o.w); *(u32x2*)(xbout + c) = w; }
;             if (xlout) { u32x2 w; w.x = pk2(o.x - bf2f(f2bf(o.x)), o.y - bf2f(f2bf(o.y))); w.y = pk2(o.z - bf2f(f2bf(o.z)), o.w - bf2f(f2bf(o.w))); *(u32x2*)(xlout + c) = w; }
;             if (x8out) *(unsigned*)(x8out + c) = pk4_fp8(o.x, o.y, o.z, o.w);
	v_and_b32_sdwa v91, v149, v222 dst_sel:DWORD dst_unused:UNUSED_PAD src0_sel:WORD_1 src1_sel:DWORD
	v_and_b32_sdwa v95, v147, v222 dst_sel:DWORD dst_unused:UNUSED_PAD src0_sel:WORD_1 src1_sel:DWORD
	v_and_b32_sdwa v119, v146, v222 dst_sel:DWORD dst_unused:UNUSED_PAD src0_sel:WORD_1 src1_sel:DWORD
	v_and_b32_sdwa v93, v148, v222 dst_sel:DWORD dst_unused:UNUSED_PAD src0_sel:WORD_1 src1_sel:DWORD
	v_add3_u32 v95, v147, v95, s30
	v_add3_u32 v119, v146, v119, s30
	v_add3_u32 v93, v148, v93, s30
	v_add3_u32 v91, v149, v91, s30
	v_and_b32_e32 v95, 0xffff0000, v95
	v_and_b32_e32 v119, 0xffff0000, v119
	v_or_b32_sdwa v147, v95, v91 dst_sel:DWORD dst_unused:UNUSED_PAD src0_sel:DWORD src1_sel:WORD_1
	v_or_b32_sdwa v146, v119, v93 dst_sel:DWORD dst_unused:UNUSED_PAD src0_sel:DWORD src1_sel:WORD_1
	v_med3_f32 v95, v144, s33, v229
	v_med3_f32 v119, v142, s33, v229
	v_mov_b32_e32 v121, 0
	v_cvt_pk_fp8_f32 v121, v119, v95
	v_pk_mul_f32 v[140:141], v[140:141], v[124:125] op_sel_hi:[1,0]
	v_med3_f32 v91, v143, s33, v229
	v_med3_f32 v93, v145, s33, v229
	v_pk_fma_f32 v[140:141], v[30:31], v[140:141], v[28:29]
	v_cvt_pk_fp8_f32 v121, v93, v91 op_sel:[0,0,1]
	v_pk_mul_f32 v[138:139], v[138:139], v[124:125] op_sel_hi:[1,0]
	v_and_b32_sdwa v93, v140, v222 dst_sel:DWORD dst_unused:UNUSED_PAD src0_sel:WORD_1 src1_sel:DWORD
	v_pk_fma_f32 v[138:139], v[26:27], v[138:139], v[24:25]
	v_add3_u32 v93, v140, v93, s30
	v_and_b32_e32 v142, 0xffff0000, v93
	v_and_b32_sdwa v93, v139, v222 dst_sel:DWORD dst_unused:UNUSED_PAD src0_sel:WORD_1 src1_sel:DWORD
	v_and_b32_sdwa v91, v141, v222 dst_sel:DWORD dst_unused:UNUSED_PAD src0_sel:WORD_1 src1_sel:DWORD
	v_and_b32_sdwa v95, v138, v222 dst_sel:DWORD dst_unused:UNUSED_PAD src0_sel:WORD_1 src1_sel:DWORD
	v_add3_u32 v93, v139, v93, s30
	v_add3_u32 v91, v141, v91, s30
	v_add3_u32 v95, v138, v95, s30
	v_and_b32_e32 v143, 0xffff0000, v93
	v_or_b32_sdwa v145, v143, v91 dst_sel:DWORD dst_unused:UNUSED_PAD src0_sel:DWORD src1_sel:WORD_1
	v_or_b32_sdwa v144, v95, v142 dst_sel:DWORD dst_unused:UNUSED_PAD src0_sel:WORD_1 src1_sel:DWORD
	global_store_dwordx2 v[116:117], v[146:147], off offset:1024
	global_store_dword v[112:113], v121, off offset:512
	global_store_dwordx2 v[114:115], v[144:145], off offset:1536
	v_and_b32_e32 v145, 0xffff0000, v91
	v_and_b32_e32 v144, 0xffff0000, v95
	v_mov_b32_e32 v146, v138
	v_mov_b32_e32 v147, v141
	v_pk_add_f32 v[144:145], v[146:147], v[144:145] neg_lo:[0,1] neg_hi:[0,1]
	v_mov_b32_e32 v146, v140
	v_mov_b32_e32 v147, v139
	v_pk_add_f32 v[142:143], v[146:147], v[142:143] neg_lo:[0,1] neg_hi:[0,1]
	v_and_b32_sdwa v91, v145, v222 dst_sel:DWORD dst_unused:UNUSED_PAD src0_sel:WORD_1 src1_sel:DWORD
	v_and_b32_sdwa v95, v143, v222 dst_sel:DWORD dst_unused:UNUSED_PAD src0_sel:WORD_1 src1_sel:DWORD
	v_and_b32_sdwa v119, v142, v222 dst_sel:DWORD dst_unused:UNUSED_PAD src0_sel:WORD_1 src1_sel:DWORD
	v_and_b32_sdwa v93, v144, v222 dst_sel:DWORD dst_unused:UNUSED_PAD src0_sel:WORD_1 src1_sel:DWORD
	v_add3_u32 v95, v143, v95, s30
	v_add3_u32 v119, v142, v119, s30
	v_add3_u32 v93, v144, v93, s30
	v_add3_u32 v91, v145, v91, s30
	v_and_b32_e32 v95, 0xffff0000, v95
	v_and_b32_e32 v119, 0xffff0000, v119
	v_or_b32_sdwa v143, v95, v91 dst_sel:DWORD dst_unused:UNUSED_PAD src0_sel:DWORD src1_sel:WORD_1
	v_or_b32_sdwa v142, v119, v93 dst_sel:DWORD dst_unused:UNUSED_PAD src0_sel:DWORD src1_sel:WORD_1
	v_med3_f32 v95, v140, s33, v229
	v_med3_f32 v119, v138, s33, v229
	v_mov_b32_e32 v121, 0
	v_cvt_pk_fp8_f32 v121, v119, v95
	v_pk_mul_f32 v[136:137], v[136:137], v[124:125] op_sel_hi:[1,0]
	v_med3_f32 v91, v139, s33, v229
	v_med3_f32 v93, v141, s33, v229
	v_pk_fma_f32 v[136:137], v[38:39], v[136:137], v[36:37]
	v_cvt_pk_fp8_f32 v121, v93, v91 op_sel:[0,0,1]
	v_pk_mul_f32 v[134:135], v[134:135], v[124:125] op_sel_hi:[1,0]
	v_and_b32_sdwa v93, v136, v222 dst_sel:DWORD dst_unused:UNUSED_PAD src0_sel:WORD_1 src1_sel:DWORD
	v_pk_fma_f32 v[134:135], v[34:35], v[134:135], v[32:33]
	v_add3_u32 v93, v136, v93, s30
	v_and_b32_e32 v138, 0xffff0000, v93
	v_and_b32_sdwa v93, v135, v222 dst_sel:DWORD dst_unused:UNUSED_PAD src0_sel:WORD_1 src1_sel:DWORD
	v_and_b32_sdwa v91, v137, v222 dst_sel:DWORD dst_unused:UNUSED_PAD src0_sel:WORD_1 src1_sel:DWORD
	v_and_b32_sdwa v95, v134, v222 dst_sel:DWORD dst_unused:UNUSED_PAD src0_sel:WORD_1 src1_sel:DWORD
	v_add3_u32 v93, v135, v93, s30
	v_add3_u32 v91, v137, v91, s30
	v_add3_u32 v95, v134, v95, s30
	v_and_b32_e32 v139, 0xffff0000, v93
	v_or_b32_sdwa v141, v139, v91 dst_sel:DWORD dst_unused:UNUSED_PAD src0_sel:DWORD src1_sel:WORD_1
	v_or_b32_sdwa v140, v95, v138 dst_sel:DWORD dst_unused:UNUSED_PAD src0_sel:WORD_1 src1_sel:DWORD
	global_store_dwordx2 v[116:117], v[142:143], off offset:1536
	global_store_dword v[112:113], v121, off offset:768
	global_store_dwordx2 v[114:115], v[140:141], off offset:2048
	v_and_b32_e32 v141, 0xffff0000, v91
	v_and_b32_e32 v140, 0xffff0000, v95
	v_mov_b32_e32 v142, v134
	v_mov_b32_e32 v143, v137
	v_pk_add_f32 v[140:141], v[142:143], v[140:141] neg_lo:[0,1] neg_hi:[0,1]
	v_mov_b32_e32 v142, v136
	v_mov_b32_e32 v143, v135
	v_pk_add_f32 v[138:139], v[142:143], v[138:139] neg_lo:[0,1] neg_hi:[0,1]
	v_and_b32_sdwa v91, v141, v222 dst_sel:DWORD dst_unused:UNUSED_PAD src0_sel:WORD_1 src1_sel:DWORD
	v_and_b32_sdwa v95, v139, v222 dst_sel:DWORD dst_unused:UNUSED_PAD src0_sel:WORD_1 src1_sel:DWORD
	v_and_b32_sdwa v119, v138, v222 dst_sel:DWORD dst_unused:UNUSED_PAD src0_sel:WORD_1 src1_sel:DWORD
	v_and_b32_sdwa v93, v140, v222 dst_sel:DWORD dst_unused:UNUSED_PAD src0_sel:WORD_1 src1_sel:DWORD
	v_add3_u32 v95, v139, v95, s30
	v_add3_u32 v119, v138, v119, s30
	v_add3_u32 v93, v140, v93, s30
; __device__ __forceinline__ float bf2f(unsigned b) { return __uint_as_float(b << 16); }
; __device__ __forceinline__ unsigned f2bf(float f) { unsigned u = __float_as_uint(f); return (u + 0x7fffu + ((u >> 16) & 1u)) >> 16; }
; __device__ __forceinline__ unsigned pk2(float lo, float hi) { return f2bf(lo) | (f2bf(hi) << 16); }
; __device__ __forceinline__ unsigned pk4_fp8(float a, float b, float c, float d) { unsigned w = 0u; w = __builtin_amdgcn_cvt_pk_fp8_f32(clamp8(a), clamp8(b), w, false); w = __builtin_amdgcn_cvt_pk_fp8_f32(clamp8(c), clamp8(d), w, true); return w; }
; template <int MAP>
; __device__ __forceinline__ void ln_finish(float (&v)[32], const float* __restrict__ g, const float* __restrict__ b, float* xout, bf16* xbout, int lane, bf16* xlout = nullptr, unsigned char* x8out = nullptr, unsigned char* xi8out = nullptr, float* sxout = nullptr) {
;     ...
;             else { const f32x4 gv = *(const f32x4*)(g + c), bv = *(const f32x4*)(b + c);
;                 o.x = v[4 * j] * rstd * gv.x + bv.x; o.y = v[4 * j + 1] * rstd * gv.y + bv.y; o.z = v[4 * j + 2] * rstd * gv.z + bv.z; o.w = v[4 * j + 3] * rstd * gv.w + bv.w; }
;             if (xout) *(f32x4*)(xout + c) = o;
;             if (xbout) { u32x2 w; w.x = pk2(o.x, o.y); w.y = pk2(o.z, o.w); *(u32x2*)(xbout + c) = w; }
;             if (xlout) { u32x2 w; w.x = pk2(o.x - bf2f(f2bf(o.x)), o.y - bf2f(f2bf(o.y))); w.y = pk2(o.z - bf2f(f2bf(o.z)), o.w - bf2f(f2bf(o.w))); *(u32x2*)(xlout + c) = w; }
;             if (x8out) *(unsigned*)(x8out + c) = pk4_fp8(o.x, o.y, o.z, o.w);
	v_add3_u32 v91, v141, v91, s30
	v_and_b32_e32 v95, 0xffff0000, v95
	v_and_b32_e32 v119, 0xffff0000, v119
	v_or_b32_sdwa v139, v95, v91 dst_sel:DWORD dst_unused:UNUSED_PAD src0_sel:DWORD src1_sel:WORD_1
	v_or_b32_sdwa v138, v119, v93 dst_sel:DWORD dst_unused:UNUSED_PAD src0_sel:DWORD src1_sel:WORD_1
	v_med3_f32 v95, v136, s33, v229
	v_med3_f32 v119, v134, s33, v229
	v_mov_b32_e32 v121, 0
	v_cvt_pk_fp8_f32 v121, v119, v95
	v_pk_mul_f32 v[132:133], v[132:133], v[124:125] op_sel_hi:[1,0]
	v_med3_f32 v91, v135, s33, v229
	v_med3_f32 v93, v137, s33, v229
	v_pk_fma_f32 v[132:133], v[46:47], v[132:133], v[44:45]
	v_cvt_pk_fp8_f32 v121, v93, v91 op_sel:[0,0,1]
	v_pk_mul_f32 v[130:131], v[130:131], v[124:125] op_sel_hi:[1,0]
	v_and_b32_sdwa v93, v132, v222 dst_sel:DWORD dst_unused:UNUSED_PAD src0_sel:WORD_1 src1_sel:DWORD
	v_pk_fma_f32 v[130:131], v[42:43], v[130:131], v[40:41]
	v_add3_u32 v93, v132, v93, s30
	v_and_b32_e32 v134, 0xffff0000, v93
	v_and_b32_sdwa v93, v131, v222 dst_sel:DWORD dst_unused:UNUSED_PAD src0_sel:WORD_1 src1_sel:DWORD
	v_and_b32_sdwa v91, v133, v222 dst_sel:DWORD dst_unused:UNUSED_PAD src0_sel:WORD_1 src1_sel:DWORD
	v_and_b32_sdwa v95, v130, v222 dst_sel:DWORD dst_unused:UNUSED_PAD src0_sel:WORD_1 src1_sel:DWORD
	v_add3_u32 v93, v131, v93, s30
	v_add3_u32 v91, v133, v91, s30
	v_add3_u32 v95, v130, v95, s30
	v_and_b32_e32 v135, 0xffff0000, v93
	v_or_b32_sdwa v137, v135, v91 dst_sel:DWORD dst_unused:UNUSED_PAD src0_sel:DWORD src1_sel:WORD_1
	v_or_b32_sdwa v136, v95, v134 dst_sel:DWORD dst_unused:UNUSED_PAD src0_sel:WORD_1 src1_sel:DWORD
	global_store_dwordx2 v[116:117], v[138:139], off offset:2048
	global_store_dword v[112:113], v121, off offset:1024
	global_store_dwordx2 v[114:115], v[136:137], off offset:2560
	v_and_b32_e32 v137, 0xffff0000, v91
	v_and_b32_e32 v136, 0xffff0000, v95
	v_mov_b32_e32 v138, v130
	v_mov_b32_e32 v139, v133
	v_pk_add_f32 v[136:137], v[138:139], v[136:137] neg_lo:[0,1] neg_hi:[0,1]
	v_mov_b32_e32 v138, v132
	v_mov_b32_e32 v139, v131
	v_pk_add_f32 v[134:135], v[138:139], v[134:135] neg_lo:[0,1] neg_hi:[0,1]
	v_and_b32_sdwa v91, v137, v222 dst_sel:DWORD dst_unused:UNUSED_PAD src0_sel:WORD_1 src1_sel:DWORD
	v_and_b32_sdwa v95, v135, v222 dst_sel:DWORD dst_unused:UNUSED_PAD src0_sel:WORD_1 src1_sel:DWORD
	v_and_b32_sdwa v119, v134, v222 dst_sel:DWORD dst_unused:UNUSED_PAD src0_sel:WORD_1 src1_sel:DWORD
	v_and_b32_sdwa v93, v136, v222 dst_sel:DWORD dst_unused:UNUSED_PAD src0_sel:WORD_1 src1_sel:DWORD
	v_add3_u32 v95, v135, v95, s30
	v_add3_u32 v119, v134, v119, s30
	v_add3_u32 v93, v136, v93, s30
	v_add3_u32 v91, v137, v91, s30
	v_and_b32_e32 v95, 0xffff0000, v95
	v_and_b32_e32 v119, 0xffff0000, v119
	v_or_b32_sdwa v135, v95, v91 dst_sel:DWORD dst_unused:UNUSED_PAD src0_sel:DWORD src1_sel:WORD_1
	v_or_b32_sdwa v134, v119, v93 dst_sel:DWORD dst_unused:UNUSED_PAD src0_sel:DWORD src1_sel:WORD_1
	v_med3_f32 v95, v132, s33, v229
	v_med3_f32 v119, v130, s33, v229
	v_mov_b32_e32 v121, 0
	v_cvt_pk_fp8_f32 v121, v119, v95
	v_pk_mul_f32 v[128:129], v[128:129], v[124:125] op_sel_hi:[1,0]
	v_med3_f32 v91, v131, s33, v229
	v_med3_f32 v93, v133, s33, v229
	v_pk_fma_f32 v[128:129], v[102:103], v[128:129], v[100:101]
	v_cvt_pk_fp8_f32 v121, v93, v91 op_sel:[0,0,1]
	v_pk_mul_f32 v[126:127], v[126:127], v[124:125] op_sel_hi:[1,0]
	v_and_b32_sdwa v93, v128, v222 dst_sel:DWORD dst_unused:UNUSED_PAD src0_sel:WORD_1 src1_sel:DWORD
	v_pk_fma_f32 v[126:127], v[98:99], v[126:127], v[96:97]
	v_add3_u32 v93, v128, v93, s30
	v_and_b32_e32 v130, 0xffff0000, v93
	v_and_b32_sdwa v93, v127, v222 dst_sel:DWORD dst_unused:UNUSED_PAD src0_sel:WORD_1 src1_sel:DWORD
	v_and_b32_sdwa v91, v129, v222 dst_sel:DWORD dst_unused:UNUSED_PAD src0_sel:WORD_1 src1_sel:DWORD
	v_and_b32_sdwa v95, v126, v222 dst_sel:DWORD dst_unused:UNUSED_PAD src0_sel:WORD_1 src1_sel:DWORD
	v_add3_u32 v93, v127, v93, s30
	v_add3_u32 v91, v129, v91, s30
	v_add3_u32 v95, v126, v95, s30
	v_and_b32_e32 v131, 0xffff0000, v93
	v_or_b32_sdwa v133, v131, v91 dst_sel:DWORD dst_unused:UNUSED_PAD src0_sel:DWORD src1_sel:WORD_1
	v_or_b32_sdwa v132, v95, v130 dst_sel:DWORD dst_unused:UNUSED_PAD src0_sel:WORD_1 src1_sel:DWORD
	global_store_dwordx2 v[116:117], v[134:135], off offset:2560
	global_store_dword v[112:113], v121, off offset:1280
	global_store_dwordx2 v[114:115], v[132:133], off offset:3072
	v_and_b32_e32 v133, 0xffff0000, v91
	v_and_b32_e32 v132, 0xffff0000, v95
	v_mov_b32_e32 v134, v126
	v_mov_b32_e32 v135, v129
	v_pk_add_f32 v[132:133], v[134:135], v[132:133] neg_lo:[0,1] neg_hi:[0,1]
	v_mov_b32_e32 v134, v128
	v_mov_b32_e32 v135, v127
	v_pk_add_f32 v[130:131], v[134:135], v[130:131] neg_lo:[0,1] neg_hi:[0,1]
	v_and_b32_sdwa v91, v133, v222 dst_sel:DWORD dst_unused:UNUSED_PAD src0_sel:WORD_1 src1_sel:DWORD
	v_and_b32_sdwa v95, v131, v222 dst_sel:DWORD dst_unused:UNUSED_PAD src0_sel:WORD_1 src1_sel:DWORD
; __device__ __forceinline__ float bf2f(unsigned b) { return __uint_as_float(b << 16); }
; __device__ __forceinline__ unsigned f2bf(float f) { unsigned u = __float_as_uint(f); return (u + 0x7fffu + ((u >> 16) & 1u)) >> 16; }
; __device__ __forceinline__ unsigned pk2(float lo, float hi) { return f2bf(lo) | (f2bf(hi) << 16); }
; __device__ __forceinline__ unsigned pk4_fp8(float a, float b, float c, float d) { unsigned w = 0u; w = __builtin_amdgcn_cvt_pk_fp8_f32(clamp8(a), clamp8(b), w, false); w = __builtin_amdgcn_cvt_pk_fp8_f32(clamp8(c), clamp8(d), w, true); return w; }
; template <int MAP>
; __device__ __forceinline__ void ln_finish(float (&v)[32], const float* __restrict__ g, const float* __restrict__ b, float* xout, bf16* xbout, int lane, bf16* xlout = nullptr, unsigned char* x8out = nullptr, unsigned char* xi8out = nullptr, float* sxout = nullptr) {
;     ...
;                 o.x = v[4 * j] * rstd * gv.x + bv.x; o.y = v[4 * j + 1] * rstd * gv.y + bv.y; o.z = v[4 * j + 2] * rstd * gv.z + bv.z; o.w = v[4 * j + 3] * rstd * gv.w + bv.w; }
;             if (xout) *(f32x4*)(xout + c) = o;
;             if (xbout) { u32x2 w; w.x = pk2(o.x, o.y); w.y = pk2(o.z, o.w); *(u32x2*)(xbout + c) = w; }
;             if (xlout) { u32x2 w; w.x = pk2(o.x - bf2f(f2bf(o.x)), o.y - bf2f(f2bf(o.y))); w.y = pk2(o.z - bf2f(f2bf(o.z)), o.w - bf2f(f2bf(o.w))); *(u32x2*)(xlout + c) = w; }
;             if (x8out) *(unsigned*)(x8out + c) = pk4_fp8(o.x, o.y, o.z, o.w);
; __device__ __forceinline__ void ln1_router_unit(const Params& p, int l, int unit, LAS unsigned char* lds, int tid, bool dry = false) {
;     ...
;     if (tid < 64) cnt[tid] = 0;
;     __threadfence_block();
;     __syncthreads();
;     {
;         const int fr = lane & 15, fq = lane >> 4;
;         const bf16* wrh = (const bf16*)(p.ws + WS_WR) + (size_t)l * 2 * NE * D; const bf16* wrl = wrh + (size_t)NE * D;
;         f32x4 racc[2][4];
; #pragma unroll
;         for (int a2 = 0; a2 < 2; ++a2)
; #pragma unroll
;             for (int b2 = 0; b2 < 4; ++b2) racc[a2][b2] = (f32x4){0.f, 0.f, 0.f, 0.f};
; #pragma unroll 2
;         for (int ks = 0; ks < 8; ++ks) {
;             const int k0 = 256 * wid + 32 * ks + 8 * fq;
	v_and_b32_sdwa v119, v130, v222 dst_sel:DWORD dst_unused:UNUSED_PAD src0_sel:WORD_1 src1_sel:DWORD
	v_and_b32_sdwa v93, v132, v222 dst_sel:DWORD dst_unused:UNUSED_PAD src0_sel:WORD_1 src1_sel:DWORD
	v_add3_u32 v95, v131, v95, s30
	v_add3_u32 v119, v130, v119, s30
	v_add3_u32 v93, v132, v93, s30
	v_add3_u32 v91, v133, v91, s30
	v_and_b32_e32 v95, 0xffff0000, v95
	v_and_b32_e32 v119, 0xffff0000, v119
	v_or_b32_sdwa v131, v95, v91 dst_sel:DWORD dst_unused:UNUSED_PAD src0_sel:DWORD src1_sel:WORD_1
	v_or_b32_sdwa v130, v119, v93 dst_sel:DWORD dst_unused:UNUSED_PAD src0_sel:DWORD src1_sel:WORD_1
	v_med3_f32 v95, v128, s33, v229
	v_med3_f32 v119, v126, s33, v229
	v_mov_b32_e32 v121, 0
	v_cvt_pk_fp8_f32 v121, v119, v95
	v_med3_f32 v91, v127, s33, v229
	v_med3_f32 v93, v129, s33, v229
	v_mov_b32_e32 v119, v123
	v_cvt_pk_fp8_f32 v121, v93, v91 op_sel:[0,0,1]
	v_pk_mul_f32 v[118:119], v[118:119], v[124:125] op_sel_hi:[1,0]
	global_store_dwordx2 v[116:117], v[130:131], off offset:3072
	v_pk_fma_f32 v[118:119], v[110:111], v[118:119], v[108:109]
	global_store_dword v[112:113], v121, off offset:1536
	v_mov_b32_e32 v121, v122
	v_pk_mul_f32 v[120:121], v[120:121], v[124:125] op_sel_hi:[1,0]
	v_and_b32_sdwa v93, v118, v222 dst_sel:DWORD dst_unused:UNUSED_PAD src0_sel:WORD_1 src1_sel:DWORD
	v_pk_fma_f32 v[120:121], v[106:107], v[120:121], v[104:105]
	v_add3_u32 v93, v118, v93, s30
	v_and_b32_e32 v122, 0xffff0000, v93
	v_and_b32_sdwa v93, v121, v222 dst_sel:DWORD dst_unused:UNUSED_PAD src0_sel:WORD_1 src1_sel:DWORD
	v_and_b32_sdwa v91, v119, v222 dst_sel:DWORD dst_unused:UNUSED_PAD src0_sel:WORD_1 src1_sel:DWORD
	v_and_b32_sdwa v95, v120, v222 dst_sel:DWORD dst_unused:UNUSED_PAD src0_sel:WORD_1 src1_sel:DWORD
	v_add3_u32 v93, v121, v93, s30
	v_add3_u32 v91, v119, v91, s30
	v_add3_u32 v95, v120, v95, s30
	v_and_b32_e32 v123, 0xffff0000, v93
	v_or_b32_sdwa v127, v123, v91 dst_sel:DWORD dst_unused:UNUSED_PAD src0_sel:DWORD src1_sel:WORD_1
	v_or_b32_sdwa v126, v95, v122 dst_sel:DWORD dst_unused:UNUSED_PAD src0_sel:WORD_1 src1_sel:DWORD
	global_store_dwordx2 v[114:115], v[126:127], off offset:3584
	v_and_b32_e32 v115, 0xffff0000, v91
	v_and_b32_e32 v114, 0xffff0000, v95
	v_mov_b32_e32 v126, v120
	v_mov_b32_e32 v127, v119
	v_pk_add_f32 v[114:115], v[126:127], v[114:115] neg_lo:[0,1] neg_hi:[0,1]
	v_mov_b32_e32 v126, v118
	v_mov_b32_e32 v127, v121
	v_pk_add_f32 v[122:123], v[126:127], v[122:123] neg_lo:[0,1] neg_hi:[0,1]
	v_and_b32_sdwa v93, v114, v222 dst_sel:DWORD dst_unused:UNUSED_PAD src0_sel:WORD_1 src1_sel:DWORD
	v_add3_u32 v93, v114, v93, s30
	v_and_b32_sdwa v95, v123, v222 dst_sel:DWORD dst_unused:UNUSED_PAD src0_sel:WORD_1 src1_sel:DWORD
	v_and_b32_sdwa v114, v122, v222 dst_sel:DWORD dst_unused:UNUSED_PAD src0_sel:WORD_1 src1_sel:DWORD
	v_and_b32_sdwa v91, v115, v222 dst_sel:DWORD dst_unused:UNUSED_PAD src0_sel:WORD_1 src1_sel:DWORD
	v_add3_u32 v95, v123, v95, s30
	v_add3_u32 v114, v122, v114, s30
	v_add3_u32 v91, v115, v91, s30
	v_and_b32_e32 v95, 0xffff0000, v95
	v_and_b32_e32 v114, 0xffff0000, v114
	v_or_b32_sdwa v115, v95, v91 dst_sel:DWORD dst_unused:UNUSED_PAD src0_sel:DWORD src1_sel:WORD_1
	v_or_b32_sdwa v114, v114, v93 dst_sel:DWORD dst_unused:UNUSED_PAD src0_sel:DWORD src1_sel:WORD_1
	global_store_dwordx2 v[116:117], v[114:115], off offset:3584
	v_med3_f32 v95, v118, s33, v229
	v_med3_f32 v114, v120, s33, v229
	v_mov_b32_e32 v115, 0
	v_cvt_pk_fp8_f32 v115, v114, v95
	v_med3_f32 v91, v121, s33, v229
	v_med3_f32 v93, v119, s33, v229
	v_cvt_pk_fp8_f32 v115, v93, v91 op_sel:[0,0,1]
	global_store_dword v[112:113], v115, off offset:1792
	s_cbranch_scc0 .LBB0_872
	s_mov_b64 s[6:7], exec
	v_readlane_b32 s12, v254, 30
	v_readlane_b32 s13, v254, 31
	s_and_b64 s[12:13], s[6:7], s[12:13]
	s_mov_b64 exec, s[12:13]
	ds_write_b32 v155, v65
	s_or_b64 exec, exec, s[6:7]
	s_lshl_b32 s15, s31, 5
	v_or_b32_e32 v0, s15, v156
	v_ashrrev_i32_e32 v1, 31, v0
	v_lshlrev_b64 v[96:97], 11, v[0:1]
	v_or_b32_e32 v0, 16, v0
	v_lshl_or_b32 v100, s8, 8, v157
	v_ashrrev_i32_e32 v1, 31, v0
	v_ashrrev_i32_e32 v101, 31, v100
	v_mov_b32_e32 v16, 0
	v_lshlrev_b64 v[98:99], 11, v[0:1]
	v_lshl_add_u64 v[102:103], v[100:101], 1, v[78:79]
	s_mov_b64 s[6:7], 0
	v_mov_b32_e32 v17, v16
	v_mov_b32_e32 v18, v16
	v_mov_b32_e32 v19, v16
	v_mov_b32_e32 v0, v16
	v_mov_b32_e32 v1, v16
	v_mov_b32_e32 v2, v16
	v_mov_b32_e32 v3, v16
	v_mov_b32_e32 v4, v16
	v_mov_b32_e32 v5, v16
	v_mov_b32_e32 v6, v16
	v_mov_b32_e32 v7, v16
	v_mov_b32_e32 v24, v16
	v_mov_b32_e32 v25, v16
	v_mov_b32_e32 v26, v16
	v_mov_b32_e32 v27, v16
	v_mov_b32_e32 v20, v16
	v_mov_b32_e32 v21, v16
	v_mov_b32_e32 v22, v16
	v_mov_b32_e32 v23, v16
	v_mov_b32_e32 v12, v16
	v_mov_b32_e32 v13, v16
	v_mov_b32_e32 v14, v16
	v_mov_b32_e32 v15, v16
	v_mov_b32_e32 v8, v16
	v_mov_b32_e32 v9, v16
	v_mov_b32_e32 v10, v16
	v_mov_b32_e32 v11, v16
	v_mov_b32_e32 v28, v16
	v_mov_b32_e32 v29, v16
	v_mov_b32_e32 v30, v16
	v_mov_b32_e32 v31, v16
	s_waitcnt lgkmcnt(0)
	s_barrier
